# speedup vs baseline: 1.0114x; 1.0114x over previous
.LBB5_4:
	v_lshrrev_b32_e32 v154, 6, v0
	v_and_b32_e32 v155, 63, v0
	s_waitcnt vmcnt(8) lgkmcnt(0)
	s_barrier
	v_mfma_f32_32x32x16_f16 v[50:65], v[130:133], v[142:145], v[50:65]
	s_lshl_b32 s4, s14, 15
	s_and_b32 s5, s4, 0x10000
	s_add_i32 s2, s5, 0
	v_add_u32_e32 v156, s2, v173
	v_add_u32_e32 v160, s2, v176
	s_mov_b32 s3, 0
	v_mfma_f32_32x32x16_f16 v[34:49], v[130:133], v[138:141], v[34:49]
	v_add_u32_e32 v130, s2, v171
	v_mfma_f32_32x32x16_f16 v[18:33], v[126:129], v[142:145], v[18:33]
	v_add_u32_e32 v142, s2, v177
	v_add_u32_e32 v143, s2, v175
	v_mfma_f32_32x32x16_f16 v[2:17], v[126:129], v[138:141], v[2:17]
	v_add_u32_e32 v138, s2, v174
	ds_read_b128 v[126:129], v130 offset:32768
	ds_read_b128 v[130:133], v130 offset:36864
	v_mfma_f32_32x32x16_f16 v[50:65], v[134:137], v[122:125], v[50:65]
	v_mfma_f32_32x32x16_f16 v[34:49], v[134:137], v[118:121], v[34:49]
	v_add_u32_e32 v134, s2, v172
	ds_read_b128 v[134:137], v134 offset:49152
	ds_read_b128 v[138:141], v138 offset:49152
	v_mfma_f32_32x32x16_f16 v[18:33], v[114:117], v[122:125], v[18:33]
	ds_read_b128 v[122:125], v142 offset:32768
	ds_read_b128 v[142:145], v143 offset:32768
	ds_read_b128 v[156:159], v156 offset:32768
	ds_read_b128 v[160:163], v160 offset:32768
	v_mfma_f32_32x32x16_f16 v[2:17], v[114:117], v[118:121], v[2:17]
	s_waitcnt vmcnt(4) lgkmcnt(0)
	s_barrier
	v_mfma_f32_32x32x16_f16 v[50:65], v[126:129], v[134:137], v[50:65]
	s_xor_b32 s2, s5, 0x10000
	s_add_i32 s2, s2, 0
	v_add_u32_e32 v118, s2, v171
	v_add_u32_e32 v146, s2, v176
	ds_read_b128 v[114:117], v118
	ds_read_b128 v[118:121], v118 offset:4096
	v_mfma_f32_32x32x16_f16 v[34:49], v[126:129], v[138:141], v[34:49]
	v_add_u32_e32 v126, s2, v174
	v_mfma_f32_32x32x16_f16 v[18:33], v[130:133], v[134:137], v[18:33]
	v_add_u32_e32 v134, s2, v175
	v_mfma_f32_32x32x16_f16 v[2:17], v[130:133], v[138:141], v[2:17]
	v_add_u32_e32 v130, s2, v177
	v_add_u32_e32 v138, s2, v173
	v_mfma_f32_32x32x16_f16 v[50:65], v[122:125], v[156:159], v[50:65]
	v_mfma_f32_32x32x16_f16 v[34:49], v[122:125], v[160:163], v[34:49]
	v_add_u32_e32 v122, s2, v172
	ds_read_b128 v[122:125], v122 offset:16384
	ds_read_b128 v[126:129], v126 offset:16384
	ds_read_b128 v[130:133], v130
	ds_read_b128 v[134:137], v134
	ds_read_b128 v[138:141], v138
	ds_read_b128 v[146:149], v146
	v_mfma_f32_32x32x16_f16 v[18:33], v[142:145], v[156:159], v[18:33]
	v_mfma_f32_32x32x16_f16 v[2:17], v[142:145], v[160:163], v[2:17]
	s_waitcnt vmcnt(0) lgkmcnt(0)
	s_barrier
	v_mfma_f32_32x32x16_f16 v[50:65], v[114:117], v[122:125], v[50:65]
	s_add_i32 s4, s4, 0x18000
	s_and_b32 s2, s4, 0x18000
	s_add_i32 s2, s2, 0
	v_add_u32_e32 v142, s2, v173
	v_add_u32_e32 v150, s2, v176
	v_mfma_f32_32x32x16_f16 v[34:49], v[114:117], v[126:129], v[34:49]
	v_mfma_f32_32x32x16_f16 v[18:33], v[118:121], v[122:125], v[18:33]
	v_add_u32_e32 v122, s2, v172
	v_mfma_f32_32x32x16_f16 v[2:17], v[118:121], v[126:129], v[2:17]
	v_add_u32_e32 v118, s2, v171
	v_add_u32_e32 v126, s2, v174
	ds_read_b128 v[114:117], v118
	ds_read_b128 v[118:121], v118 offset:4096
	ds_read_b128 v[122:125], v122 offset:16384
	ds_read_b128 v[126:129], v126 offset:16384
	v_mfma_f32_32x32x16_f16 v[50:65], v[130:133], v[138:141], v[50:65]
	v_mfma_f32_32x32x16_f16 v[34:49], v[130:133], v[146:149], v[34:49]
	v_add_u32_e32 v130, s2, v177
	v_mfma_f32_32x32x16_f16 v[18:33], v[134:137], v[138:141], v[18:33]
	v_add_u32_e32 v138, s2, v175
	ds_read_b128 v[130:133], v130
	ds_read_b128 v[138:141], v138
	ds_read_b128 v[142:145], v142
	ds_read_b128 v[150:153], v150
	v_mfma_f32_32x32x16_f16 v[2:17], v[134:137], v[146:149], v[2:17]
	s_waitcnt vmcnt(0) lgkmcnt(0)
	s_barrier
	v_mfma_f32_32x32x16_f16 v[50:65], v[114:117], v[122:125], v[50:65]
	v_mfma_f32_32x32x16_f16 v[34:49], v[114:117], v[126:129], v[34:49]
	v_mfma_f32_32x32x16_f16 v[18:33], v[118:121], v[122:125], v[18:33]
	v_mfma_f32_32x32x16_f16 v[2:17], v[118:121], v[126:129], v[2:17]
	v_mfma_f32_32x32x16_f16 v[50:65], v[130:133], v[142:145], v[50:65]
	v_mfma_f32_32x32x16_f16 v[34:49], v[130:133], v[150:153], v[34:49]
	v_mfma_f32_32x32x16_f16 v[18:33], v[138:141], v[142:145], v[18:33]
	v_mfma_f32_32x32x16_f16 v[2:17], v[138:141], v[150:153], v[2:17]
	s_waitcnt vmcnt(0) lgkmcnt(0)
	s_movk_i32 s2, 0x100
	s_movk_i32 s4, 0xff
	v_lshl_add_u32 v114, v155, 2, 0
	v_cmp_gt_u32_e64 s[2:3], s2, v0
	v_cmp_lt_u32_e32 vcc, s4, v0
	v_lshlrev_b32_e32 v0, 14, v1
	s_and_saveexec_b64 s[4:5], vcc
	s_cbranch_execz .LBB5_6
	v_add3_u32 v1, v114, v0, v169
	ds_write2st64_b32 v1, v50, v51 offset1:1
	ds_write2st64_b32 v1, v52, v53 offset0:2 offset1:3
	ds_write2st64_b32 v1, v54, v55 offset0:4 offset1:5
	ds_write2st64_b32 v1, v56, v57 offset0:6 offset1:7
	ds_write2st64_b32 v1, v58, v59 offset0:8 offset1:9
	ds_write2st64_b32 v1, v60, v61 offset0:10 offset1:11
	ds_write2st64_b32 v1, v62, v63 offset0:12 offset1:13
	ds_write2st64_b32 v1, v64, v65 offset0:14 offset1:15
	ds_write2st64_b32 v1, v34, v35 offset0:16 offset1:17
	ds_write2st64_b32 v1, v36, v37 offset0:18 offset1:19
	ds_write2st64_b32 v1, v38, v39 offset0:20 offset1:21
	ds_write2st64_b32 v1, v40, v41 offset0:22 offset1:23
	ds_write2st64_b32 v1, v42, v43 offset0:24 offset1:25
	ds_write2st64_b32 v1, v44, v45 offset0:26 offset1:27
	ds_write2st64_b32 v1, v46, v47 offset0:28 offset1:29
	ds_write2st64_b32 v1, v48, v49 offset0:30 offset1:31

.LBB6_4:
	v_lshrrev_b32_e32 v80, 6, v0
	v_and_b32_e32 v81, 63, v0
	s_waitcnt vmcnt(3) lgkmcnt(0)
	s_barrier
	v_mfma_f32_32x32x16_f16 v[18:33], v[66:69], v[70:73], v[18:33]
	s_and_b32 s4, s10, 2
	s_mul_i32 s2, s4, 0x6000
	s_add_i32 s2, s2, 0
	v_add_u32_e32 v66, s2, v94
	v_add_u32_e32 v82, s2, v97
	v_add_u32_e32 v86, s2, v98
	s_mov_b32 s3, 0
	v_mfma_f32_32x32x16_f16 v[2:17], v[62:65], v[70:73], v[2:17]
	v_add_u32_e32 v70, s2, v95
	v_add_u32_e32 v71, s2, v96
	ds_read_b128 v[62:65], v66 offset:24576
	ds_read_b128 v[66:69], v66 offset:28672
	v_mfma_f32_32x32x16_f16 v[18:33], v[58:61], v[54:57], v[18:33]
	ds_read_b128 v[58:61], v70 offset:40960
	ds_read_b128 v[70:73], v71 offset:24576
	ds_read_b128 v[82:85], v82 offset:24576
	ds_read_b128 v[100:103], v86 offset:24576
	v_mfma_f32_32x32x16_f16 v[2:17], v[50:53], v[54:57], v[2:17]
	s_add_i32 s2, s10, 3
	s_and_b32 s5, s2, 3
	s_mulk_i32 s5, 0x6000
	s_add_i32 s5, s5, 0
	v_add_u32_e32 v52, s5, v93
	s_lshl_b64 s[2:3], s[2:3], 7
	v_readfirstlane_b32 s6, v52
	v_add_u32_e32 v53, 0x2000, v52
	v_lshl_add_u64 v[50:51], v[74:75], 0, s[2:3]
	s_mov_b32 m0, s6
	v_readfirstlane_b32 s6, v53
	global_load_lds_dwordx4 v[50:51], off
	v_lshl_add_u64 v[50:51], v[76:77], 0, s[2:3]
	s_mov_b32 m0, s6
	v_add_u32_e32 v52, 0x4000, v52
	global_load_lds_dwordx4 v[50:51], off
	v_lshl_add_u64 v[50:51], v[78:79], 0, s[2:3]
	v_readfirstlane_b32 s2, v52
	s_mov_b32 m0, s2
	s_nop 0
	global_load_lds_dwordx4 v[50:51], off
	s_waitcnt vmcnt(3) lgkmcnt(0)
	s_barrier
	v_mfma_f32_32x32x16_f16 v[18:33], v[62:65], v[58:61], v[18:33]
	s_xor_b32 s2, s4, 2
	s_mulk_i32 s2, 0x6000
	s_add_i32 s2, s2, 0
	v_add_u32_e32 v54, s2, v94
	v_add_u32_e32 v62, s2, v96
	ds_read_b128 v[50:53], v54
	ds_read_b128 v[54:57], v54 offset:4096
	v_mfma_f32_32x32x16_f16 v[2:17], v[66:69], v[58:61], v[2:17]
	v_add_u32_e32 v58, s2, v95
	v_add_u32_e32 v66, s2, v97
	ds_read_b128 v[58:61], v58 offset:16384
	ds_read_b128 v[62:65], v62
	v_mfma_f32_32x32x16_f16 v[18:33], v[70:73], v[100:103], v[18:33]
	v_add_u32_e32 v70, s2, v98
	ds_read_b128 v[66:69], v66
	ds_read_b128 v[70:73], v70
	v_mfma_f32_32x32x16_f16 v[2:17], v[82:85], v[100:103], v[2:17]
	s_waitcnt vmcnt(0) lgkmcnt(0)
	s_barrier
	v_mfma_f32_32x32x16_f16 v[18:33], v[50:53], v[58:61], v[18:33]
	v_add_u32_e32 v74, s5, v97
	v_add_u32_e32 v78, s5, v98
	v_mfma_f32_32x32x16_f16 v[2:17], v[54:57], v[58:61], v[2:17]
	v_add_u32_e32 v54, s5, v94
	v_add_u32_e32 v58, s5, v95
	ds_read_b128 v[50:53], v54
	ds_read_b128 v[54:57], v54 offset:4096
	v_mfma_f32_32x32x16_f16 v[18:33], v[62:65], v[70:73], v[18:33]
	v_add_u32_e32 v62, s5, v96
	ds_read_b128 v[58:61], v58 offset:16384
	ds_read_b128 v[62:65], v62
	ds_read_b128 v[74:77], v74
	ds_read_b128 v[82:85], v78
	v_mfma_f32_32x32x16_f16 v[2:17], v[66:69], v[70:73], v[2:17]
	s_waitcnt vmcnt(0) lgkmcnt(0)
	s_barrier
	v_mfma_f32_32x32x16_f16 v[18:33], v[50:53], v[58:61], v[18:33]
	v_mfma_f32_32x32x16_f16 v[2:17], v[54:57], v[58:61], v[2:17]
	v_mfma_f32_32x32x16_f16 v[18:33], v[62:65], v[82:85], v[18:33]
	v_mfma_f32_32x32x16_f16 v[2:17], v[74:77], v[82:85], v[2:17]
	s_waitcnt vmcnt(0) lgkmcnt(0)
	v_lshlrev_b32_e32 v1, 1, v1
	s_movk_i32 s2, 0x100
	s_movk_i32 s4, 0xff
	v_lshl_add_u32 v50, v81, 2, 0
	v_cmp_gt_u32_e64 s[2:3], s2, v0
	v_cmp_lt_u32_e32 vcc, s4, v0
	v_or_b32_e32 v0, v1, v92
	v_lshl_add_u32 v0, v0, 12, v50
	s_and_saveexec_b64 s[4:5], vcc
	s_cbranch_execz .LBB6_6
	ds_write2st64_b32 v0, v18, v19 offset1:1
	ds_write2st64_b32 v0, v20, v21 offset0:2 offset1:3
	ds_write2st64_b32 v0, v22, v23 offset0:4 offset1:5
	ds_write2st64_b32 v0, v24, v25 offset0:6 offset1:7
	ds_write2st64_b32 v0, v26, v27 offset0:8 offset1:9
	ds_write2st64_b32 v0, v28, v29 offset0:10 offset1:11
	ds_write2st64_b32 v0, v30, v31 offset0:12 offset1:13
	ds_write2st64_b32 v0, v32, v33 offset0:14 offset1:15

.LBB7_3:
	v_and_b32_e32 v53, 63, v0
	v_lshrrev_b32_e32 v54, 6, v0
	v_accvgpr_read_b32 v56, a16
	v_accvgpr_read_b32 v57, a17
	v_accvgpr_read_b32 v58, a18
	v_accvgpr_read_b32 v59, a19
	v_accvgpr_read_b32 v60, a20
	v_accvgpr_read_b32 v61, a21
	v_accvgpr_read_b32 v62, a22
	v_accvgpr_read_b32 v63, a23
	v_accvgpr_read_b32 v64, a24
	v_accvgpr_read_b32 v65, a25
	v_accvgpr_read_b32 v66, a26
	v_accvgpr_read_b32 v67, a27
	v_accvgpr_read_b32 v68, a28
	v_accvgpr_read_b32 v69, a29
	v_accvgpr_read_b32 v70, a30
	v_accvgpr_read_b32 v71, a31
	s_waitcnt vmcnt(4) lgkmcnt(0)
	s_barrier
	v_accvgpr_mov_b32 a31, a15
	v_accvgpr_mov_b32 a30, a14
	v_accvgpr_mov_b32 a29, a13
	v_accvgpr_mov_b32 a28, a12
	v_accvgpr_mov_b32 a27, a11
	v_accvgpr_mov_b32 a26, a10
	v_accvgpr_mov_b32 a25, a9
	v_accvgpr_mov_b32 a24, a8
	v_accvgpr_mov_b32 a23, a7
	v_accvgpr_mov_b32 a22, a6
	v_accvgpr_mov_b32 a21, a5
	v_accvgpr_mov_b32 a20, a4
	v_accvgpr_mov_b32 a19, a3
	v_accvgpr_mov_b32 a18, a2
	v_accvgpr_mov_b32 a17, a1
	v_accvgpr_mov_b32 a16, a0
	v_accvgpr_write_b32 a0, v56
	v_accvgpr_write_b32 a1, v57
	v_accvgpr_write_b32 a2, v58
	v_accvgpr_write_b32 a3, v59
	v_accvgpr_write_b32 a4, v60
	v_accvgpr_write_b32 a5, v61
	v_accvgpr_write_b32 a6, v62
	v_accvgpr_write_b32 a7, v63
	v_accvgpr_write_b32 a8, v64
	v_accvgpr_write_b32 a9, v65
	v_accvgpr_write_b32 a10, v66
	v_accvgpr_write_b32 a11, v67
	v_accvgpr_write_b32 a12, v68
	v_accvgpr_write_b32 a13, v69
	v_accvgpr_write_b32 a14, v70
	v_accvgpr_write_b32 a15, v71
	s_lshl_b32 s4, s17, 14
	s_and_b32 s5, s4, 0x8000
	v_mfma_f32_32x32x16_f16 a[0:15], v[80:83], v[88:91], a[0:15]
	s_add_i32 s2, s5, 0
	v_add_u32_e32 v14, s2, v22
	v_add_u32_e32 v18, s2, v23
	ds_read_b128 v[10:13], v14 offset:16384
	ds_read_b128 v[14:17], v14 offset:20480
	v_add_u32_e32 v19, s2, v24
	ds_read_b128 v[56:59], v18 offset:24576
	ds_read_b128 v[60:63], v19 offset:16384
	v_add_u32_e32 v18, s2, v25
	v_mfma_f32_32x32x16_f16 a[16:31], v[84:87], v[88:91], a[16:31]
	v_add_u32_e32 v19, s2, v26
	ds_read_b128 v[64:67], v18 offset:16384
	ds_read_b128 v[68:71], v19 offset:16384
	s_mov_b32 s3, 0
	v_mfma_f32_32x32x16_f16 a[0:15], v[28:31], v[72:75], a[0:15]
	v_mfma_f32_32x32x16_f16 a[16:31], v[76:79], v[72:75], a[16:31]
	s_add_i32 s2, s17, 3
	s_lshl_b32 s6, s2, 14
	s_and_b32 s6, s6, 0xc000
	s_add_i32 s6, s6, 0
	v_add_u32_e32 v18, s6, v20
	s_lshl_b64 s[2:3], s[2:3], 7
	v_readfirstlane_b32 s6, v18
	v_lshl_add_u64 v[2:3], v[2:3], 0, s[2:3]
	s_mov_b32 m0, s6
	s_nop 0
	global_load_lds_dwordx4 v[2:3], off
	v_lshl_add_u64 v[2:3], v[4:5], 0, s[2:3]
	v_add_u32_e32 v4, 0x1000, v18
	s_nop 0
	v_readfirstlane_b32 s6, v4
	v_add_u32_e32 v4, 0x2000, v18
	s_mov_b32 m0, s6
	v_readfirstlane_b32 s6, v4
	global_load_lds_dwordx4 v[2:3], off
	v_lshl_add_u64 v[2:3], v[6:7], 0, s[2:3]
	s_mov_b32 m0, s6
	v_add_u32_e32 v4, 0x3000, v18
	global_load_lds_dwordx4 v[2:3], off
	v_lshl_add_u64 v[2:3], v[8:9], 0, s[2:3]
	v_readfirstlane_b32 s2, v4
	s_mov_b32 m0, s2
	s_nop 0
	global_load_lds_dwordx4 v[2:3], off
	s_waitcnt vmcnt(4) lgkmcnt(0)
	s_barrier
	v_mfma_f32_32x32x16_f16 a[0:15], v[14:17], v[56:59], a[0:15]
	s_xor_b32 s2, s5, 0x8000
	s_add_i32 s2, s2, 0
	v_add_u32_e32 v6, s2, v22
	v_add_u32_e32 v14, s2, v24
	v_add_u32_e32 v18, s2, v25
	ds_read_b128 v[2:5], v6
	ds_read_b128 v[6:9], v6 offset:4096
	v_add_u32_e32 v19, s2, v26
	v_mfma_f32_32x32x16_f16 a[16:31], v[10:13], v[56:59], a[16:31]
	v_add_u32_e32 v10, s2, v23
	ds_read_b128 v[10:13], v10 offset:8192
	ds_read_b128 v[14:17], v14
	ds_read_b128 v[28:31], v18
	ds_read_b128 v[56:59], v19
	v_mfma_f32_32x32x16_f16 a[0:15], v[64:67], v[68:71], a[0:15]
	v_mfma_f32_32x32x16_f16 a[16:31], v[60:63], v[68:71], a[16:31]
	s_waitcnt vmcnt(0) lgkmcnt(0)
	s_barrier
	v_mfma_f32_32x32x16_f16 a[0:15], v[6:9], v[10:13], a[0:15]
	s_add_i32 s4, s4, 0xc000
	s_and_b32 s2, s4, 0xc000
	s_add_i32 s2, s2, 0
	v_add_u32_e32 v6, s2, v22
	v_add_u32_e32 v18, s2, v25
	v_add_u32_e32 v19, s2, v26
	v_mfma_f32_32x32x16_f16 a[16:31], v[2:5], v[10:13], a[16:31]
	v_add_u32_e32 v10, s2, v23
	ds_read_b128 v[2:5], v6
	ds_read_b128 v[6:9], v6 offset:4096
	v_mfma_f32_32x32x16_f16 a[0:15], v[28:31], v[56:59], a[0:15]
	v_mfma_f32_32x32x16_f16 a[16:31], v[14:17], v[56:59], a[16:31]
	v_add_u32_e32 v14, s2, v24
	ds_read_b128 v[10:13], v10 offset:8192
	ds_read_b128 v[14:17], v14
	ds_read_b128 v[22:25], v18
	ds_read_b128 v[60:63], v19
	s_waitcnt vmcnt(0) lgkmcnt(0)
	s_barrier
	v_mfma_f32_32x32x16_f16 a[16:31], v[2:5], v[10:13], a[16:31]
	v_mfma_f32_32x32x16_f16 a[0:15], v[6:9], v[10:13], a[0:15]
	v_mfma_f32_32x32x16_f16 a[16:31], v[14:17], v[60:63], a[16:31]
	v_mfma_f32_32x32x16_f16 a[0:15], v[22:25], v[60:63], a[0:15]
	s_nop 10
	v_accvgpr_read_b32 v2, a16
	v_accvgpr_read_b32 v3, a17
	v_accvgpr_read_b32 v4, a18
	v_accvgpr_read_b32 v5, a19
	v_accvgpr_read_b32 v6, a20
	v_accvgpr_read_b32 v7, a21
	v_accvgpr_read_b32 v8, a22
	v_accvgpr_read_b32 v9, a23
	v_accvgpr_read_b32 v10, a24
	v_accvgpr_read_b32 v11, a25
	v_accvgpr_read_b32 v12, a26
	v_accvgpr_read_b32 v13, a27
	v_accvgpr_read_b32 v14, a28
	v_accvgpr_read_b32 v15, a29
	v_accvgpr_read_b32 v16, a30
	v_accvgpr_read_b32 v17, a31
	s_waitcnt vmcnt(0) lgkmcnt(0)
	s_movk_i32 s2, 0x80
	v_lshlrev_b32_e32 v18, 2, v53
	v_cmp_gt_u32_e64 s[4:5], s2, v0
	s_movk_i32 s2, 0x7f
	v_add3_u32 v55, 0, v21, v18
	v_cmp_lt_u32_e32 vcc, s2, v0
	s_and_saveexec_b64 s[2:3], vcc
	s_cbranch_execz .LBB7_5
	ds_write2st64_b32 v55, v2, v3 offset1:1
	ds_write2st64_b32 v55, v4, v5 offset0:2 offset1:3
	ds_write2st64_b32 v55, v6, v7 offset0:4 offset1:5
	ds_write2st64_b32 v55, v8, v9 offset0:6 offset1:7
	ds_write2st64_b32 v55, v10, v11 offset0:8 offset1:9
	ds_write2st64_b32 v55, v12, v13 offset0:10 offset1:11
	ds_write2st64_b32 v55, v14, v15 offset0:12 offset1:13
	ds_write2st64_b32 v55, v16, v17 offset0:14 offset1:15
